# speedup vs baseline: 1.0484x; 1.0040x over previous
.LBB0_3:
	s_load_dwordx8 s[20:27], s[0:1], 0x68
	v_and_b32_e32 v2, 31, v0
	s_lshr_b32 s3, s2, 3
	s_and_b32 s30, s2, 7
	v_cmp_gt_u32_e64 s[10:11], 21, v2
	s_mul_i32 s30, s30, 0x30000
	v_lshrrev_b32_e32 v6, 5, v0
	v_cndmask_b32_e64 v1, 0, v2, s[10:11]
	s_cmpk_gt_u32 s2, 0x41f
	s_cbranch_scc0 .LBB0_11
	s_cmpk_gt_u32 s2, 0x45f
	s_cbranch_scc0 .LBB0_8
	s_load_dwordx2 s[28:29], s[0:1], 0x60
	s_load_dwordx2 s[18:19], s[0:1], 0x48
	s_load_dwordx2 s[8:9], s[0:1], 0x38
	s_load_dwordx2 s[32:33], s[0:1], 0x40
	s_load_dwordx4 s[36:39], s[0:1], 0x50
	v_lshrrev_b32_e32 v3, 2, v2
	v_and_b32_e32 v2, 28, v2
	v_and_b32_e32 v7, 3, v0
	v_and_b32_e32 v51, 7, v0
	v_lshlrev_b32_e32 v51, 2, v51
	s_waitcnt lgkmcnt(0)
	global_load_dword v52, v51, s[28:29]
	global_load_dword v53, v51, s[32:33]
	global_load_dword v54, v51, s[38:39]
	global_load_dword v55, v51, s[36:37]
	global_load_dword v51, v51, s[18:19]
	global_load_dword v22, v2, s[18:19]
	global_load_dword v23, v2, s[28:29]
	v_cmp_lt_u32_e32 vcc, 31, v0
	v_mul_u32_u24_e32 v24, 27, v3
	v_sub_u32_e32 v27, 2, v7
	v_cndmask_b32_e64 v2, 0, 1, vcc
	v_sub_co_u32_e32 v26, vcc, 1, v7
	v_max_i32_e32 v8, 0, v26
	v_lshl_add_u32 v8, v8, 3, v8
	v_sub_u32_e32 v16, 4, v7
	v_add_lshl_u32 v4, v24, v2, 2
	v_mov_b32_e32 v5, 0
	v_ashrrev_i32_e32 v9, 31, v8
	v_max_i32_e32 v12, 0, v27
	v_min_u32_e32 v16, 2, v16
	v_lshl_add_u64 v[2:3], s[8:9], 0, v[4:5]
	v_lshlrev_b64 v[8:9], 2, v[8:9]
	v_mul_u32_u24_e32 v12, 9, v12
	v_mul_u32_u24_e32 v16, 9, v16
	v_lshl_add_u64 v[10:11], v[2:3], 0, v[8:9]
	v_lshlrev_b32_e32 v12, 2, v12
	v_mov_b32_e32 v13, v5
	v_lshlrev_b32_e32 v16, 2, v16
	v_mov_b32_e32 v17, v5
	global_load_dword v25, v4, s[8:9]
	v_lshl_add_u64 v[14:15], v[2:3], 0, v[12:13]
	v_lshl_add_u64 v[18:19], v[2:3], 0, v[16:17]
	global_load_dword v28, v[10:11], off
	global_load_dword v29, v[14:15], off
	global_load_dword v30, v[18:19], off
	v_bitop3_b32 v10, v0, 3, v0 bitop3:0xc
	v_min_u32_e32 v10, 2, v10
	v_mul_u32_u24_e32 v10, 9, v10
	v_lshlrev_b32_e32 v10, 2, v10
	v_mov_b32_e32 v11, v5
	v_lshl_add_u64 v[2:3], v[2:3], 0, v[10:11]
	v_cmp_gt_u32_e64 s[4:5], 32, v0
	global_load_dword v31, v[2:3], off
	global_load_dword v32, v4, s[8:9] offset:72
	v_cndmask_b32_e64 v2, 4, 3, s[4:5]
	v_add_lshl_u32 v4, v2, v24, 2
	v_lshl_add_u64 v[2:3], s[8:9], 0, v[4:5]
	v_lshl_add_u64 v[14:15], v[2:3], 0, v[8:9]
	global_load_dword v33, v4, s[8:9]
	global_load_dword v34, v[14:15], off
	v_lshl_add_u64 v[14:15], v[2:3], 0, v[12:13]
	v_lshl_add_u64 v[18:19], v[2:3], 0, v[10:11]
	v_lshl_add_u64 v[2:3], v[2:3], 0, v[16:17]
	global_load_dword v35, v[14:15], off
	global_load_dword v36, v[18:19], off
	global_load_dword v37, v[2:3], off
	global_load_dword v38, v4, s[8:9] offset:72
	v_cndmask_b32_e64 v2, 8, 7, s[4:5]
	v_add_lshl_u32 v4, v2, v24, 2
	v_lshl_add_u64 v[2:3], s[8:9], 0, v[4:5]
	v_lshl_add_u64 v[14:15], v[2:3], 0, v[8:9]
	v_lshl_add_u64 v[18:19], v[2:3], 0, v[12:13]
	v_lshl_add_u64 v[20:21], v[2:3], 0, v[10:11]
	v_lshl_add_u64 v[2:3], v[2:3], 0, v[16:17]
	global_load_dword v39, v4, s[8:9]
	global_load_dword v40, v[14:15], off
	global_load_dword v41, v[18:19], off
	global_load_dword v42, v[20:21], off
	global_load_dword v43, v[2:3], off
	global_load_dword v44, v4, s[8:9] offset:72
	v_cndmask_b32_e64 v2, 5, 2, s[4:5]
	v_add_lshl_u32 v4, v2, v24, 2
	v_lshl_add_u64 v[2:3], s[8:9], 0, v[4:5]
	v_lshl_add_u64 v[14:15], v[2:3], 0, v[8:9]
	v_lshl_add_u64 v[18:19], v[2:3], 0, v[12:13]
	v_lshl_add_u64 v[20:21], v[2:3], 0, v[10:11]
	v_lshl_add_u64 v[2:3], v[2:3], 0, v[16:17]
	global_load_dword v45, v[14:15], off
	global_load_dword v46, v[18:19], off
	global_load_dword v47, v[20:21], off
	global_load_dword v48, v[2:3], off
	global_load_dword v49, v4, s[8:9]
	global_load_dword v50, v4, s[8:9] offset:72
	v_cndmask_b32_e64 v2, 8, 6, s[4:5]
	v_add_lshl_u32 v4, v2, v24, 2
	s_mov_b32 s31, 0x800000
	v_lshl_add_u64 v[2:3], s[8:9], 0, v[4:5]
	v_lshl_add_u64 v[8:9], v[2:3], 0, v[8:9]
	v_lshl_add_u64 v[12:13], v[2:3], 0, v[12:13]
	v_lshl_add_u64 v[10:11], v[2:3], 0, v[10:11]
	v_lshl_add_u64 v[2:3], v[2:3], 0, v[16:17]
	v_cmp_gt_u32_e64 s[12:13], 3, v27
	v_cmp_ne_u32_e64 s[14:15], 0, v7
	v_cmp_eq_u32_e64 s[16:17], 3, v7
	s_add_u32 s24, s24, s30
	s_addc_u32 s25, s25, 0
	s_waitcnt vmcnt(24)
	v_add_f32_e32 v14, 0x3727c5ac, v23
	v_mul_f32_e32 v15, 0x4b800000, v14
	v_cmp_gt_f32_e64 s[6:7], s31, v14
	s_nop 1
	v_cndmask_b32_e64 v14, v14, v15, s[6:7]
	global_load_dword v15, v4, s[8:9]
	global_load_dword v16, v[8:9], off
	global_load_dword v17, v[12:13], off
	global_load_dword v18, v[10:11], off
	global_load_dword v19, v4, s[8:9] offset:72
	global_load_dword v20, v[2:3], off
	v_rsq_f32_e32 v14, v14
	v_cmp_gt_u32_e64 s[8:9], 3, v26
	v_mul_f32_e32 v2, 0x45800000, v14
	v_cndmask_b32_e64 v2, v14, v2, s[6:7]
	v_mul_f32_e32 v12, v22, v2
	v_cmp_eq_u32_e64 s[6:7], 0, v7
	s_waitcnt vmcnt(29)
	v_fma_mixlo_f16 v2, v12, v25, 0
	s_waitcnt vmcnt(28)
	v_fma_mixlo_f16 v3, v12, v28, 0
	v_cndmask_b32_e64 v8, 0, v3, s[8:9]
	s_waitcnt vmcnt(26)
	v_fma_mixlo_f16 v4, v12, v30, 0
	v_fma_mixlo_f16 v3, v12, v29, 0
	v_cndmask_b32_e64 v2, 0, v2, s[6:7]
	v_cndmask_b32_e32 v4, 0, v4, vcc
	v_cndmask_b32_e64 v3, 0, v3, s[12:13]
	v_pack_b32_f16 v2, v2, v8
	v_lshlrev_b32_e32 v8, 4, v0
	s_waitcnt vmcnt(25)
	v_fma_mixlo_f16 v9, v12, v31, 0
	s_waitcnt vmcnt(24)
	v_fma_mixlo_f16 v10, v12, v32, 0
	v_cndmask_b32_e64 v9, 0, v9, s[14:15]
	v_cndmask_b32_e64 v7, 0, v10, s[16:17]
	v_pack_b32_f16 v4, v4, v7
	v_pack_b32_f16 v3, v3, v9
	v_mov_b32_e32 v9, v5
	global_store_dwordx4 v8, v[2:5], s[24:25]
	v_lshl_add_u64 v[10:11], s[24:25], 0, v[8:9]
	s_waitcnt vmcnt(19)
	v_fma_mixlo_f16 v13, v12, v38, 0
	v_fma_mixlo_f16 v3, v12, v34, 0
	v_fma_mixlo_f16 v4, v12, v36, 0
	v_fma_mixlo_f16 v2, v12, v33, 0
	v_cndmask_b32_e64 v7, 0, v3, s[8:9]
	v_fma_mixlo_f16 v3, v12, v35, 0
	v_cndmask_b32_e64 v9, 0, v4, s[14:15]
	v_fma_mixlo_f16 v4, v12, v37, 0
	v_cndmask_b32_e64 v2, 0, v2, s[6:7]
	v_cndmask_b32_e64 v3, 0, v3, s[12:13]
	v_cndmask_b32_e32 v4, 0, v4, vcc
	v_cndmask_b32_e64 v13, 0, v13, s[16:17]
	v_pack_b32_f16 v4, v4, v13
	v_pack_b32_f16 v3, v3, v9
	v_pack_b32_f16 v2, v2, v7
	global_store_dwordx4 v8, v[2:5], s[24:25] offset:1024
	s_waitcnt vmcnt(14)
	v_fma_mixlo_f16 v13, v12, v44, 0
	v_cndmask_b32_e64 v13, 0, v13, s[16:17]
	v_fma_mixlo_f16 v3, v12, v40, 0
	v_fma_mixlo_f16 v4, v12, v42, 0
	v_fma_mixlo_f16 v2, v12, v39, 0
	v_cndmask_b32_e64 v7, 0, v3, s[8:9]
	v_fma_mixlo_f16 v3, v12, v41, 0
	v_cndmask_b32_e64 v9, 0, v4, s[14:15]
	v_fma_mixlo_f16 v4, v12, v43, 0
	v_cndmask_b32_e64 v2, 0, v2, s[6:7]
	v_cndmask_b32_e64 v3, 0, v3, s[12:13]
	v_cndmask_b32_e32 v4, 0, v4, vcc
	v_pack_b32_f16 v4, v4, v13
	v_pack_b32_f16 v3, v3, v9
	v_pack_b32_f16 v2, v2, v7
	global_store_dwordx4 v8, v[2:5], s[24:25] offset:2048
	s_waitcnt vmcnt(9)
	v_fma_mixlo_f16 v13, v12, v50, 0
	v_cndmask_b32_e64 v13, 0, v13, s[16:17]
	v_fma_mixlo_f16 v3, v12, v45, 0
	v_fma_mixlo_f16 v4, v12, v47, 0
	v_fma_mixlo_f16 v2, v12, v49, 0
	v_cndmask_b32_e64 v7, 0, v3, s[8:9]
	v_fma_mixlo_f16 v3, v12, v46, 0
	v_cndmask_b32_e64 v9, 0, v4, s[14:15]
	v_fma_mixlo_f16 v4, v12, v48, 0
	v_cndmask_b32_e64 v2, 0, v2, s[6:7]
	v_cndmask_b32_e64 v3, 0, v3, s[12:13]
	v_cndmask_b32_e32 v4, 0, v4, vcc
	v_pack_b32_f16 v4, v4, v13
	v_pack_b32_f16 v3, v3, v9
	v_pack_b32_f16 v2, v2, v7
	global_store_dwordx4 v8, v[2:5], s[24:25] offset:3072
	s_and_b64 vcc, s[4:5], vcc
	s_nop 0
	v_and_b32_e32 v2, 35, v0
	s_waitcnt vmcnt(9)
	v_fma_mixlo_f16 v3, v12, v15, 0
	v_cmp_eq_u32_e64 s[6:7], 0, v2
	s_waitcnt vmcnt(6)
	v_fma_mixlo_f16 v4, v12, v18, 0
	v_cndmask_b32_e64 v7, 0, v3, s[6:7]
	v_fma_mixlo_f16 v3, v12, v16, 0
	s_and_b64 s[6:7], s[4:5], s[8:9]
	v_cndmask_b32_e64 v8, 0, v3, s[6:7]
	v_fma_mixlo_f16 v3, v12, v17, 0
	s_and_b64 s[6:7], s[4:5], s[12:13]
	v_cndmask_b32_e64 v3, 0, v3, s[6:7]
	s_and_b64 s[6:7], s[4:5], s[14:15]
	v_cndmask_b32_e64 v9, 0, v4, s[6:7]
	s_waitcnt vmcnt(4)
	v_fma_mixlo_f16 v4, v12, v20, 0
	v_cndmask_b32_e32 v4, 0, v4, vcc
	v_fma_mixlo_f16 v12, v12, v19, 0
	v_cmp_eq_u32_e32 vcc, 3, v2
	v_pack_b32_f16 v3, v3, v9
	s_nop 0
	v_cndmask_b32_e32 v2, 0, v12, vcc
	v_pack_b32_f16 v4, v4, v2
	v_pack_b32_f16 v2, v7, v8
	v_add_co_u32_e32 v8, vcc, 0x1000, v10
	s_nop 1
	v_addc_co_u32_e32 v9, vcc, 0, v11, vcc
	v_cmp_gt_u32_e32 vcc, 8, v0
	global_store_dwordx4 v[8:9], v[2:5], off
	s_and_saveexec_b64 s[4:5], vcc
	s_cbranch_execz .LBB0_7
	s_add_u32 s6, s26, s30
	s_addc_u32 s7, s27, 0
	v_add_f32_e32 v2, 0x3727c5ac, v52
	v_mul_f32_e32 v3, 0x4b800000, v2
	v_cmp_gt_f32_e32 vcc, s31, v2
	s_nop 1
	v_cndmask_b32_e32 v2, v2, v3, vcc
	v_rsq_f32_e32 v2, v2
	v_sub_f32_e32 v3, v53, v54
	v_mul_f32_e32 v4, 0x45800000, v2
	v_cndmask_b32_e32 v2, v2, v4, vcc
	v_mul_f32_e32 v2, v51, v2
	v_fmac_f32_e32 v55, v3, v2
	v_lshlrev_b32_e32 v2, 2, v0
	global_store_dword v2, v55, s[6:7]

.LBB0_8:
	s_andn2_b64 vcc, exec, s[4:5]
	s_cbranch_vccnz .LBB0_10
	s_load_dwordx8 s[12:19], s[0:1], 0x18
	s_waitcnt lgkmcnt(0)
	s_add_u32 s22, s22, s30
	s_addc_u32 s23, s23, 0
	s_add_i32 s26, s3, 0xffffff7c
	s_lshr_b32 s4, s26, 1
	s_cmp_eq_u32 s4, 2
	s_cselect_b32 s5, s17, s19
	s_cselect_b32 s6, s16, s18
	s_cmp_eq_u32 s4, 1
	s_cselect_b32 s4, s14, s6
	s_cselect_b32 s5, s15, s5
	s_cmp_lt_u32 s26, 2
	s_cselect_b32 s25, s13, s5
	s_cselect_b32 s24, s12, s4
	s_lshl_b32 s4, s3, 4
	v_lshlrev_b32_e32 v2, 3, v6
	v_and_or_b32 v7, s4, 16, v2
	v_mul_u32_u24_e32 v2, 21, v7
	v_cmp_gt_u32_e32 vcc, 21, v7
	v_mad_u32_u24 v3, v7, 21, 21
	v_or_b32_e32 v4, 2, v7
	v_cndmask_b32_e32 v2, 0, v2, vcc
	v_add_lshl_u32 v12, v2, v1, 2
	v_or_b32_e32 v2, 1, v7
	v_cmp_gt_u32_e64 s[4:5], 21, v2
	v_mad_u32_u24 v5, v7, 21, 42
	v_cmp_gt_u32_e64 s[6:7], 21, v4
	v_cndmask_b32_e64 v2, 0, v3, s[4:5]
	v_add_u32_e32 v8, v2, v1
	v_mov_b32_e32 v9, 0
	v_cndmask_b32_e64 v4, 0, v5, s[6:7]
	v_lshl_add_u64 v[2:3], v[8:9], 2, s[24:25]
	v_add_u32_e32 v8, v4, v1
	v_lshl_add_u64 v[4:5], v[8:9], 2, s[24:25]
	v_or_b32_e32 v8, 3, v7
	v_mad_u32_u24 v10, v7, 21, 63
	v_cmp_gt_u32_e64 s[8:9], 21, v8
	s_and_b64 vcc, vcc, s[10:11]
	s_nop 0
	v_cndmask_b32_e64 v8, 0, v10, s[8:9]
	v_add_u32_e32 v8, v8, v1
	v_lshl_add_u64 v[10:11], v[8:9], 2, s[24:25]
	global_load_dword v13, v12, s[24:25]
	global_load_dword v14, v[2:3], off
	global_load_dword v15, v[4:5], off
	global_load_dword v16, v[10:11], off
	v_or_b32_e32 v2, 4, v7
	v_mov_b32_e32 v3, 0x54
	v_mad_u32_u24 v3, v7, 21, v3
	v_cmp_gt_u32_e64 s[12:13], 21, v2
	v_or_b32_e32 v4, 5, v7
	v_mov_b32_e32 v5, 0x69
	v_cndmask_b32_e64 v2, 0, v3, s[12:13]
	v_mad_u32_u24 v5, v7, 21, v5
	v_cmp_gt_u32_e64 s[14:15], 21, v4
	v_add_u32_e32 v8, v2, v1
	v_lshl_add_u64 v[2:3], v[8:9], 2, s[24:25]
	v_cndmask_b32_e64 v4, 0, v5, s[14:15]
	v_add_u32_e32 v8, v4, v1
	v_lshl_add_u64 v[4:5], v[8:9], 2, s[24:25]
	v_or_b32_e32 v8, 6, v7
	v_mov_b32_e32 v10, 0x7e
	v_mad_u32_u24 v10, v7, 21, v10
	v_cmp_gt_u32_e64 s[16:17], 21, v8
	s_nop 1
	v_cndmask_b32_e64 v8, 0, v10, s[16:17]
	v_add_u32_e32 v8, v8, v1
	v_lshl_add_u64 v[10:11], v[8:9], 2, s[24:25]
	global_load_dword v12, v[2:3], off
	global_load_dword v17, v[4:5], off
	global_load_dword v18, v[10:11], off
	v_or_b32_e32 v2, 7, v7
	v_mov_b32_e32 v3, 0x93
	v_mad_u32_u24 v3, v7, 21, v3
	v_cmp_gt_u32_e64 s[18:19], 21, v2
	s_nop 1
	v_cndmask_b32_e64 v2, 0, v3, s[18:19]
	v_add_u32_e32 v8, v2, v1
	v_lshl_add_u64 v[2:3], v[8:9], 2, s[24:25]
	global_load_dword v3, v[2:3], off
	s_waitcnt vmcnt(6)
	v_cvt_f16_f32_e32 v4, v14
	v_cvt_f16_f32_e32 v2, v13
	s_waitcnt vmcnt(5)
	v_cvt_f16_f32_e32 v5, v15
	s_waitcnt vmcnt(4)
	v_cvt_f16_f32_e32 v7, v16
	v_lshl_or_b32 v8, s26, 6, v0
	v_cndmask_b32_e32 v2, 0, v2, vcc
	s_and_b64 vcc, s[4:5], s[10:11]
	v_cndmask_b32_e32 v4, 0, v4, vcc
	s_and_b64 vcc, s[6:7], s[10:11]
	v_cndmask_b32_e32 v5, 0, v5, vcc
	s_and_b64 vcc, s[8:9], s[10:11]
	v_pack_b32_f16 v2, v2, v4
	v_cndmask_b32_e32 v4, 0, v7, vcc
	s_and_b64 vcc, s[12:13], s[10:11]
	v_lshl_add_u64 v[8:9], v[8:9], 4, s[22:23]
	s_waitcnt vmcnt(3)
	v_cvt_f16_f32_e32 v10, v12
	s_waitcnt vmcnt(2)
	v_cvt_f16_f32_e32 v11, v17
	s_waitcnt vmcnt(1)
	v_cvt_f16_f32_e32 v12, v18
	v_cndmask_b32_e32 v10, 0, v10, vcc
	s_and_b64 vcc, s[14:15], s[10:11]
	s_waitcnt vmcnt(0)
	v_cvt_f16_f32_e32 v7, v3
	v_pack_b32_f16 v3, v5, v4
	v_cndmask_b32_e32 v4, 0, v11, vcc
	s_and_b64 vcc, s[16:17], s[10:11]
	v_cndmask_b32_e32 v5, 0, v12, vcc
	s_and_b64 vcc, s[18:19], s[10:11]
	v_cndmask_b32_e32 v7, 0, v7, vcc
	v_pack_b32_f16 v4, v10, v4
	v_pack_b32_f16 v5, v5, v7
	global_store_dwordx4 v[8:9], v[2:5], off

	.amdhsa_kernel _Z6k_prepPKfS0_S0_S0_S0_S0_S0_S0_S0_S0_S0_S0_S0_PDv8_DF16_S2_S2_PfS0_
		.amdhsa_group_segment_fixed_size 0
		.amdhsa_private_segment_fixed_size 0
		.amdhsa_kernarg_size 144
		.amdhsa_user_sgpr_count 2
		.amdhsa_user_sgpr_dispatch_ptr 0
		.amdhsa_user_sgpr_queue_ptr 0
		.amdhsa_user_sgpr_kernarg_segment_ptr 1
		.amdhsa_user_sgpr_dispatch_id 0
		.amdhsa_user_sgpr_kernarg_preload_length 0
		.amdhsa_user_sgpr_kernarg_preload_offset 0
		.amdhsa_user_sgpr_private_segment_size 0
		.amdhsa_uses_dynamic_stack 0
		.amdhsa_enable_private_segment 0
		.amdhsa_system_sgpr_workgroup_id_x 1
		.amdhsa_system_sgpr_workgroup_id_y 0
		.amdhsa_system_sgpr_workgroup_id_z 0
		.amdhsa_system_sgpr_workgroup_info 0
		.amdhsa_system_vgpr_workitem_id 0
		.amdhsa_next_free_vgpr 56
		.amdhsa_next_free_sgpr 40
		.amdhsa_accum_offset 56
		.amdhsa_reserve_vcc 1
		.amdhsa_float_round_mode_32 0
		.amdhsa_float_round_mode_16_64 0
		.amdhsa_float_denorm_mode_32 3
		.amdhsa_float_denorm_mode_16_64 3
		.amdhsa_dx10_clamp 1
		.amdhsa_ieee_mode 1
		.amdhsa_fp16_overflow 0
		.amdhsa_tg_split 0
		.amdhsa_exception_fp_ieee_invalid_op 0
		.amdhsa_exception_fp_denorm_src 0
		.amdhsa_exception_fp_ieee_div_zero 0
		.amdhsa_exception_fp_ieee_overflow 0
		.amdhsa_exception_fp_ieee_underflow 0
		.amdhsa_exception_fp_ieee_inexact 0
		.amdhsa_exception_int_div_zero 0
	.end_amdhsa_kernel

.LBB1_21:
	s_or_b64 exec, exec, s[6:7]
	s_waitcnt lgkmcnt(0)
	s_barrier
	s_cmpk_lt_u32 s3, 0x100
	s_cbranch_scc1 .Lmy_nonp6
	s_sub_i32 s72, s42, 4
	s_lshl_b32 s72, s72, 5
	v_add_u32_e32 v1, s72, v114
	v_min_u32_e32 v2, 0x78, v1
	v_mul_u32_u24_e32 v4, 0xbb, v2
	v_lshrrev_b32_e32 v4, 11, v4
	v_mad_i32_i24 v5, v4, -11, v2
	v_sub_u32_e32 v6, 5, v4
	v_subrev_u32_e32 v7, 5, v4
	v_max_i32_e32 v6, v6, v7
	v_sub_u32_e32 v7, 5, v5
	v_subrev_u32_e32 v8, 5, v5
	v_max_i32_e32 v7, v7, v8
	v_max_i32_e32 v6, v6, v7
	v_sub_u32_e32 v7, 5, v6
	v_add_u32_e32 v8, 5, v6
	v_mul_u32_u24_e32 v9, 6, v6
	v_add_u32_e32 v9, v9, v4
	v_sub_u32_e32 v9, v9, v7
	v_lshlrev_b32_e32 v10, 2, v6
	v_add_u32_e32 v10, v10, v5
	v_sub_u32_e32 v10, v10, v7
	v_cmp_eq_u32_e32 vcc, v4, v8
	v_cmp_lt_u32_e64 s[74:75], v5, v8
	s_and_b64 vcc, vcc, s[74:75]
	v_cndmask_b32_e32 v9, v9, v10, vcc
	v_lshlrev_b32_e32 v10, 1, v6
	v_add_u32_e32 v10, v10, v4
	v_sub_u32_e32 v10, v10, v7
	v_add_u32_e32 v10, -1, v10
	v_cmp_eq_u32_e32 vcc, v5, v8
	v_cmp_gt_u32_e64 s[74:75], v4, v7
	s_and_b64 vcc, vcc, s[74:75]
	v_cndmask_b32_e32 v9, v9, v10, vcc
	v_sub_u32_e32 v10, v5, v7
	v_add_u32_e32 v10, -1, v10
	v_cmp_eq_u32_e32 vcc, v4, v7
	v_cmp_gt_u32_e64 s[74:75], v5, v7
	s_and_b64 vcc, vcc, s[74:75]
	v_cndmask_b32_e32 v9, v9, v10, vcc
	v_add_u32_e32 v10, -1, v6
	v_mul_u32_u24_e32 v10, v10, v6
	v_lshlrev_b32_e32 v10, 2, v10
	v_add3_u32 v9, v9, v10, 2
	v_cmp_ne_u32_e32 vcc, 0, v6
	s_nop 1
	v_cndmask_b32_e32 v9, 1, v9, vcc
	v_cmp_gt_u32_e32 vcc, 0x79, v1
	s_nop 1
	v_cndmask_b32_e32 v3, v1, v9, vcc
	v_cndmask_b32_e64 v12, 0, 1.0, vcc
	v_cmp_eq_u32_e32 vcc, 0x79, v1
	s_nop 1
	v_cndmask_b32_e64 v3, v3, 0, vcc
	v_cndmask_b32_e64 v14, 0, 1.0, vcc
	v_cmp_gt_u32_e32 vcc, 0x7a, v1
	s_nop 1
	v_cndmask_b32_e64 v13, 0, 1.0, vcc
	v_cmp_eq_u32_e32 vcc, 0, v115
	s_nop 1
	v_cndmask_b32_e64 v112, 52, 64, vcc
	v_min_u32_e32 v10, 0x79, v3
	v_mul_u32_u24_e32 v10, 0x54, v10
	v_lshl_add_u32 v63, v115, 4, v10
	v_add_u32_e32 v11, v63, v112
	global_load_dwordx4 v[64:67], v63, s[26:27]
	global_load_dwordx4 v[68:71], v63, s[26:27] offset:32
	global_load_dwordx4 v[72:75], v11, s[26:27]
	v_lshlrev_b32_e32 v10, 4, v115
	v_add_u32_e32 v11, v10, v112
	global_load_dwordx4 v[76:79], v10, s[28:29]
	global_load_dwordx4 v[80:83], v10, s[28:29] offset:32
	global_load_dwordx4 v[84:87], v11, s[28:29]
	v_add_u32_e32 v113, 0x12ed0, v10
	ds_read_b128 v[88:91], v113 offset:288
	ds_read_b128 v[92:95], v113 offset:320
	ds_read_b128 v[96:99], v113 offset:352
	ds_read_b128 v[100:103], v113 offset:96
	ds_read_b128 v[104:107], v113 offset:128
	ds_read_b128 v[108:111], v113 offset:160
	ds_read_b128 v[116:119], v113
	ds_read_b128 v[120:123], v113 offset:32
	ds_read_b128 v[124:127], v113 offset:64
	v_mul_u32_u24_e32 v10, 0x79, v115
	v_add_u32_e32 v10, v10, v2
	v_mul_u32_u24_e32 v60, 48, v10
	ds_read_b128 v[44:47], v60
	ds_read_b128 v[48:51], v60 offset:11616
	ds_read_b128 v[52:55], v60 offset:23232
	ds_read_b128 v[56:59], v60 offset:34848
	v_and_b32_e32 v10, 1, v114
	v_lshlrev_b32_e32 v10, 4, v10
	v_mov_b32_e32 v11, 0x3c00
	v_lshlrev_b32_e32 v61, v10, v11
	v_lshrrev_b32_e32 v62, 1, v114
	v_cmp_eq_u32_e64 s[72:73], 0, v62
	v_cmp_eq_u32_e64 s[74:75], 1, v62
	v_cmp_eq_u32_e64 s[76:77], 2, v62
	v_cmp_eq_u32_e64 s[78:79], 3, v62
	v_cmp_eq_u32_e64 s[80:81], 4, v62
	v_cmp_eq_u32_e64 s[82:83], 5, v62
	v_cmp_eq_u32_e64 s[84:85], 6, v62
	v_cmp_eq_u32_e64 s[86:87], 7, v62
	v_cmp_eq_u32_e64 s[88:89], 8, v62
	v_cmp_eq_u32_e64 s[90:91], 9, v62
	v_cmp_eq_u32_e64 s[92:93], 10, v62
	v_cmp_eq_u32_e64 s[94:95], 11, v62
	v_cndmask_b32_e64 v32, 0, v61, s[72:73]
	v_cndmask_b32_e64 v33, 0, v61, s[74:75]
	v_cndmask_b32_e64 v34, 0, v61, s[76:77]
	v_cndmask_b32_e64 v35, 0, v61, s[78:79]
	v_cndmask_b32_e64 v36, 0, v61, s[80:81]
	v_cndmask_b32_e64 v37, 0, v61, s[82:83]
	v_cndmask_b32_e64 v38, 0, v61, s[84:85]
	v_cndmask_b32_e64 v39, 0, v61, s[86:87]
	v_cndmask_b32_e64 v40, 0, v61, s[88:89]
	v_cndmask_b32_e64 v41, 0, v61, s[90:91]
	v_cndmask_b32_e64 v42, 0, v61, s[92:93]
	v_cndmask_b32_e64 v43, 0, v61, s[94:95]
	v_cmp_eq_u32_e64 s[72:73], 0, v115
	s_waitcnt lgkmcnt(3)
	v_mfma_f32_32x32x16_f16 v[16:31], v[32:35], v[44:47], 0
	ds_read_b128 v[44:47], v60 offset:16
	s_waitcnt lgkmcnt(3)
	v_mfma_f32_32x32x16_f16 v[16:31], v[32:35], v[48:51], v[16:31]
	ds_read_b128 v[48:51], v60 offset:11632
	s_waitcnt lgkmcnt(3)
	v_mfma_f32_32x32x16_f16 v[16:31], v[32:35], v[52:55], v[16:31]
	ds_read_b128 v[52:55], v60 offset:23248
	s_waitcnt lgkmcnt(3)
	v_mfma_f32_32x32x16_f16 v[16:31], v[32:35], v[56:59], v[16:31]
	ds_read_b128 v[56:59], v60 offset:34864
	s_waitcnt lgkmcnt(3)
	v_mfma_f32_32x32x16_f16 v[16:31], v[36:39], v[44:47], v[16:31]
	ds_read_b128 v[44:47], v60 offset:32
	s_waitcnt lgkmcnt(3)
	v_mfma_f32_32x32x16_f16 v[16:31], v[36:39], v[48:51], v[16:31]
	ds_read_b128 v[48:51], v60 offset:11648
	s_waitcnt lgkmcnt(3)
	v_mfma_f32_32x32x16_f16 v[16:31], v[36:39], v[52:55], v[16:31]
	ds_read_b128 v[52:55], v60 offset:23264
	s_waitcnt lgkmcnt(3)
	v_mfma_f32_32x32x16_f16 v[16:31], v[36:39], v[56:59], v[16:31]
	ds_read_b128 v[56:59], v60 offset:34880
	s_waitcnt lgkmcnt(3)
	v_mfma_f32_32x32x16_f16 v[16:31], v[40:43], v[44:47], v[16:31]
	s_waitcnt lgkmcnt(2)
	v_mfma_f32_32x32x16_f16 v[16:31], v[40:43], v[48:51], v[16:31]
	s_waitcnt lgkmcnt(1)
	v_mfma_f32_32x32x16_f16 v[16:31], v[40:43], v[52:55], v[16:31]
	s_waitcnt lgkmcnt(0)
	v_mfma_f32_32x32x16_f16 v[16:31], v[40:43], v[56:59], v[16:31]
	s_waitcnt vmcnt(0)
	v_cndmask_b32_e64 v72, v75, v72, s[72:73]
	v_cndmask_b32_e64 v84, v87, v84, s[72:73]
	v_fmac_f32_e32 v64, v14, v76
	v_fmac_f32_e32 v65, v14, v77
	v_fmac_f32_e32 v66, v14, v78
	v_fmac_f32_e32 v67, v14, v79
	v_fmac_f32_e32 v68, v14, v80
	v_fmac_f32_e32 v69, v14, v81
	v_fmac_f32_e32 v70, v14, v82
	v_fmac_f32_e32 v71, v14, v83
	v_fmac_f32_e32 v72, v14, v84
	v_fmac_f32_e32 v73, v14, v85
	v_fmac_f32_e32 v74, v14, v86
	v_fmac_f32_e32 v75, v14, v87
	v_add_f32_e32 v16, v88, v16
	v_max_f32_e32 v16, 0, v16
	v_fmac_f32_e32 v64, v16, v12
	v_mul_f32_e32 v64, v13, v64
	v_add_f32_e32 v17, v89, v17
	v_max_f32_e32 v17, 0, v17
	v_fmac_f32_e32 v65, v17, v12
	v_mul_f32_e32 v65, v13, v65
	v_add_f32_e32 v18, v90, v18
	v_max_f32_e32 v18, 0, v18
	v_fmac_f32_e32 v66, v18, v12
	v_mul_f32_e32 v66, v13, v66
	v_add_f32_e32 v19, v91, v19
	v_max_f32_e32 v19, 0, v19
	v_fmac_f32_e32 v67, v19, v12
	v_mul_f32_e32 v67, v13, v67
	v_add_f32_e32 v20, v92, v20
	v_max_f32_e32 v20, 0, v20
	v_fmac_f32_e32 v68, v20, v12
	v_mul_f32_e32 v68, v13, v68
	v_add_f32_e32 v21, v93, v21
	v_max_f32_e32 v21, 0, v21
	v_fmac_f32_e32 v69, v21, v12
	v_mul_f32_e32 v69, v13, v69
	v_add_f32_e32 v22, v94, v22
	v_max_f32_e32 v22, 0, v22
	v_fmac_f32_e32 v70, v22, v12
	v_mul_f32_e32 v70, v13, v70
	v_add_f32_e32 v23, v95, v23
	v_max_f32_e32 v23, 0, v23
	v_fmac_f32_e32 v71, v23, v12
	v_mul_f32_e32 v71, v13, v71
	v_add_f32_e32 v24, v96, v24
	v_max_f32_e32 v24, 0, v24
	v_fmac_f32_e32 v72, v24, v12
	v_mul_f32_e32 v72, v13, v72
	v_add_f32_e32 v25, v97, v25
	v_max_f32_e32 v25, 0, v25
	v_fmac_f32_e32 v73, v25, v12
	v_mul_f32_e32 v73, v13, v73
	v_add_f32_e32 v26, v98, v26
	v_max_f32_e32 v26, 0, v26
	v_fmac_f32_e32 v74, v26, v12
	v_mul_f32_e32 v74, v13, v74
	v_add_f32_e32 v27, v99, v27
	v_max_f32_e32 v27, 0, v27
	v_fmac_f32_e32 v75, v27, v12
	v_mul_f32_e32 v75, v13, v75
	v_cndmask_b32_e64 v73, 0, v73, s[72:73]
	v_cndmask_b32_e64 v74, 0, v74, s[72:73]
	v_cndmask_b32_e64 v75, 0, v75, s[72:73]
	v_mul_u32_u24_e32 v10, 0x54, v3
	v_lshl_add_u32 v10, v115, 4, v10
	v_add_u32_e32 v112, 0xb600, v10
	ds_write2_b32 v112, v64, v65 offset1:1
	ds_write2_b32 v112, v66, v67 offset0:2 offset1:3
	ds_write2_b32 v112, v68, v69 offset0:8 offset1:9
	ds_write2_b32 v112, v70, v71 offset0:10 offset1:11
	ds_write_b32 v112, v72 offset:64
	s_mov_b32 exec_hi, 0
	ds_write2_b32 v112, v73, v74 offset0:17 offset1:18
	ds_write_b32 v112, v75 offset:76
	s_mov_b32 exec_hi, -1
	v_add_f32_e32 v28, v64, v65
	v_add_f32_e32 v28, v28, v66
	v_add_f32_e32 v28, v28, v67
	v_add_f32_e32 v28, v28, v68
	v_add_f32_e32 v28, v28, v69
	v_add_f32_e32 v28, v28, v70
	v_add_f32_e32 v28, v28, v71
	v_add_f32_e32 v28, v28, v72
	v_add_f32_e32 v28, v28, v73
	v_add_f32_e32 v28, v28, v74
	v_add_f32_e32 v28, v28, v75
	v_mov_b32_e32 v29, v28
	s_nop 1
	v_permlane32_swap_b32_e32 v28, v29
	v_add_f32_e32 v28, v28, v29
	v_mul_f32_e32 v28, 0x3d430c31, v28
	v_sub_f32_e32 v64, v64, v28
	v_sub_f32_e32 v65, v65, v28
	v_sub_f32_e32 v66, v66, v28
	v_sub_f32_e32 v67, v67, v28
	v_sub_f32_e32 v68, v68, v28
	v_sub_f32_e32 v69, v69, v28
	v_sub_f32_e32 v70, v70, v28
	v_sub_f32_e32 v71, v71, v28
	v_sub_f32_e32 v72, v72, v28
	v_sub_f32_e32 v73, v73, v28
	v_sub_f32_e32 v74, v74, v28
	v_sub_f32_e32 v75, v75, v28
	v_cndmask_b32_e64 v73, 0, v73, s[72:73]
	v_cndmask_b32_e64 v74, 0, v74, s[72:73]
	v_cndmask_b32_e64 v75, 0, v75, s[72:73]
	v_mul_f32_e32 v30, v64, v64
	v_fmac_f32_e32 v30, v65, v65
	v_fmac_f32_e32 v30, v66, v66
	v_fmac_f32_e32 v30, v67, v67
	v_fmac_f32_e32 v30, v68, v68
	v_fmac_f32_e32 v30, v69, v69
	v_fmac_f32_e32 v30, v70, v70
	v_fmac_f32_e32 v30, v71, v71
	v_fmac_f32_e32 v30, v72, v72
	v_fmac_f32_e32 v30, v73, v73
	v_fmac_f32_e32 v30, v74, v74
	v_fmac_f32_e32 v30, v75, v75
	v_mov_b32_e32 v31, v30
	s_nop 1
	v_permlane32_swap_b32_e32 v30, v31
	v_add_f32_e32 v30, v30, v31
	v_mov_b32_e32 v31, 0x3727c5ac
	v_fmac_f32_e32 v31, 0x3d430c31, v30
	v_rsq_f32_e32 v31, v31
	s_nop 0
	v_mul_f32_e32 v31, v13, v31
	v_mul_f32_e32 v64, v64, v31
	v_mul_f32_e32 v116, v13, v116
	v_fmac_f32_e32 v116, v64, v100
	v_mul_f32_e32 v65, v65, v31
	v_mul_f32_e32 v117, v13, v117
	v_fmac_f32_e32 v117, v65, v101
	v_mul_f32_e32 v66, v66, v31
	v_mul_f32_e32 v118, v13, v118
	v_fmac_f32_e32 v118, v66, v102
	v_mul_f32_e32 v67, v67, v31
	v_mul_f32_e32 v119, v13, v119
	v_fmac_f32_e32 v119, v67, v103
	v_mul_f32_e32 v68, v68, v31
	v_mul_f32_e32 v120, v13, v120
	v_fmac_f32_e32 v120, v68, v104
	v_mul_f32_e32 v69, v69, v31
	v_mul_f32_e32 v121, v13, v121
	v_fmac_f32_e32 v121, v69, v105
	v_mul_f32_e32 v70, v70, v31
	v_mul_f32_e32 v122, v13, v122
	v_fmac_f32_e32 v122, v70, v106
	v_mul_f32_e32 v71, v71, v31
	v_mul_f32_e32 v123, v13, v123
	v_fmac_f32_e32 v123, v71, v107
	v_mul_f32_e32 v72, v72, v31
	v_mul_f32_e32 v124, v13, v124
	v_fmac_f32_e32 v124, v72, v108
	v_mul_f32_e32 v73, v73, v31
	v_mul_f32_e32 v125, v13, v125
	v_fmac_f32_e32 v125, v73, v109
	v_mul_f32_e32 v74, v74, v31
	v_mul_f32_e32 v126, v13, v126
	v_fmac_f32_e32 v126, v74, v110
	v_mul_f32_e32 v75, v75, v31
	v_mul_f32_e32 v127, v13, v127
	v_fmac_f32_e32 v127, v75, v111
	v_cndmask_b32_e64 v125, 0, v125, s[72:73]
	v_cndmask_b32_e64 v126, 0, v126, s[72:73]
	v_cndmask_b32_e64 v127, 0, v127, s[72:73]
	v_cvt_pk_f16_f32 v4, v116, v117
	v_cvt_pk_f16_f32 v5, v118, v119
	v_cvt_pk_f16_f32 v6, v120, v121
	v_cvt_pk_f16_f32 v7, v122, v123
	v_cvt_pk_f16_f32 v8, v124, v125
	v_cvt_pk_f16_f32 v9, v126, v127
	v_mul_u32_u24_e32 v10, 0x50, v3
	v_lshl_add_u32 v10, v115, 3, v10
	v_add_u32_e32 v113, 0xf550, v10
	ds_write_b64 v113, v[4:5]
	ds_write_b64 v113, v[6:7] offset:16
	ds_write_b64 v113, v[8:9] offset:32
	v_mov_b32_e32 v28, 0
	v_mov_b32_e32 v29, 0
	v_mov_b32_e32 v30, 0
	v_mov_b32_e32 v31, 0
	s_mov_b32 exec_hi, 0
	ds_write_b128 v113, v[28:31] offset:48
	s_mov_b32 exec_hi, -1

amdhsa.kernels:
  - .agpr_count:     0
    .args:
      - .actual_access:  read_only
        .address_space:  global
        .offset:         0
        .size:           8
        .value_kind:     global_buffer
      - .actual_access:  read_only
        .address_space:  global
        .offset:         8
        .size:           8
        .value_kind:     global_buffer
      - .actual_access:  read_only
        .address_space:  global
        .offset:         16
        .size:           8
        .value_kind:     global_buffer
      - .actual_access:  read_only
        .address_space:  global
        .offset:         24
        .size:           8
        .value_kind:     global_buffer
      - .actual_access:  read_only
        .address_space:  global
        .offset:         32
        .size:           8
        .value_kind:     global_buffer
      - .actual_access:  read_only
        .address_space:  global
        .offset:         40
        .size:           8
        .value_kind:     global_buffer
      - .actual_access:  read_only
        .address_space:  global
        .offset:         48
        .size:           8
        .value_kind:     global_buffer
      - .actual_access:  read_only
        .address_space:  global
        .offset:         56
        .size:           8
        .value_kind:     global_buffer
      - .actual_access:  read_only
        .address_space:  global
        .offset:         64
        .size:           8
        .value_kind:     global_buffer
      - .actual_access:  read_only
        .address_space:  global
        .offset:         72
        .size:           8
        .value_kind:     global_buffer
      - .actual_access:  read_only
        .address_space:  global
        .offset:         80
        .size:           8
        .value_kind:     global_buffer
      - .actual_access:  read_only
        .address_space:  global
        .offset:         88
        .size:           8
        .value_kind:     global_buffer
      - .actual_access:  read_only
        .address_space:  global
        .offset:         96
        .size:           8
        .value_kind:     global_buffer
      - .address_space:  global
        .offset:         104
        .size:           8
        .value_kind:     global_buffer
      - .address_space:  global
        .offset:         112
        .size:           8
        .value_kind:     global_buffer
      - .address_space:  global
        .offset:         120
        .size:           8
        .value_kind:     global_buffer
      - .address_space:  global
        .offset:         128
        .size:           8
        .value_kind:     global_buffer
      - .actual_access:  read_only
        .address_space:  global
        .offset:         136
        .size:           8
        .value_kind:     global_buffer
    .group_segment_fixed_size: 0
    .kernarg_segment_align: 8
    .kernarg_segment_size: 144
    .language:       OpenCL C
    .language_version:
      - 2
      - 0
    .max_flat_workgroup_size: 64
    .name:           _Z6k_prepPKfS0_S0_S0_S0_S0_S0_S0_S0_S0_S0_S0_S0_PDv8_DF16_S2_S2_PfS0_
    .private_segment_fixed_size: 0
    .sgpr_count:     46
    .sgpr_spill_count: 0
    .symbol:         _Z6k_prepPKfS0_S0_S0_S0_S0_S0_S0_S0_S0_S0_S0_S0_PDv8_DF16_S2_S2_PfS0_.kd
    .uniform_work_group_size: 1
    .uses_dynamic_stack: false
    .vgpr_count:     56
    .vgpr_spill_count: 0
    .wavefront_size: 64
  - .agpr_count:     0
    .args:
      - .actual_access:  read_only
        .address_space:  global
        .offset:         0
        .size:           8
        .value_kind:     global_buffer
      - .address_space:  global
        .offset:         8
        .size:           8
        .value_kind:     global_buffer
      - .address_space:  global
        .offset:         16
        .size:           8
        .value_kind:     global_buffer
      - .address_space:  global
        .offset:         24
        .size:           8
        .value_kind:     global_buffer
      - .actual_access:  read_only
        .address_space:  global
        .offset:         32
        .size:           8
        .value_kind:     global_buffer
      - .actual_access:  read_only
        .address_space:  global
        .offset:         40
        .size:           8
        .value_kind:     global_buffer
      - .actual_access:  read_only
        .address_space:  global
        .offset:         48
        .size:           8
        .value_kind:     global_buffer
      - .actual_access:  read_only
        .address_space:  global
        .offset:         56
        .size:           8
        .value_kind:     global_buffer
      - .actual_access:  read_only
        .address_space:  global
        .offset:         64
        .size:           8
        .value_kind:     global_buffer
      - .actual_access:  read_only
        .address_space:  global
        .offset:         72
        .size:           8
        .value_kind:     global_buffer
      - .actual_access:  read_only
        .address_space:  global
        .offset:         80
        .size:           8
        .value_kind:     global_buffer
      - .actual_access:  read_only
        .address_space:  global
        .offset:         88
        .size:           8
        .value_kind:     global_buffer
      - .actual_access:  read_only
        .address_space:  global
        .offset:         96
        .size:           8
        .value_kind:     global_buffer
      - .address_space:  global
        .offset:         104
        .size:           8
        .value_kind:     global_buffer
      - .actual_access:  read_only
        .address_space:  global
        .offset:         112
        .size:           8
        .value_kind:     global_buffer
      - .actual_access:  read_only
        .address_space:  global
        .offset:         120
        .size:           8
        .value_kind:     global_buffer
      - .actual_access:  read_only
        .address_space:  global
        .offset:         128
        .size:           8
        .value_kind:     global_buffer
      - .actual_access:  read_only
        .address_space:  global
        .offset:         136
        .size:           8
        .value_kind:     global_buffer
      - .actual_access:  read_only
        .address_space:  global
        .offset:         144
        .size:           8
        .value_kind:     global_buffer
      - .actual_access:  read_only
        .address_space:  global
        .offset:         152
        .size:           8
        .value_kind:     global_buffer
      - .actual_access:  read_only
        .address_space:  global
        .offset:         160
        .size:           8
        .value_kind:     global_buffer
      - .actual_access:  read_only
        .address_space:  global
        .offset:         168
        .size:           8
        .value_kind:     global_buffer
      - .actual_access:  read_only
        .address_space:  global
        .offset:         176
        .size:           8
        .value_kind:     global_buffer
      - .actual_access:  read_only
        .address_space:  global
        .offset:         184
        .size:           8
        .value_kind:     global_buffer
      - .actual_access:  read_only
        .address_space:  global
        .offset:         192
        .size:           8
        .value_kind:     global_buffer
      - .actual_access:  read_only
        .address_space:  global
        .offset:         200
        .size:           8
        .value_kind:     global_buffer
      - .actual_access:  read_only
        .address_space:  global
        .offset:         208
        .size:           8
        .value_kind:     global_buffer
      - .actual_access:  write_only
        .address_space:  global
        .offset:         216
        .size:           8
        .value_kind:     global_buffer
    .group_segment_fixed_size: 78032
    .kernarg_segment_align: 8
    .kernarg_segment_size: 224
    .language:       OpenCL C
    .language_version:
      - 2
      - 0
    .max_flat_workgroup_size: 512
    .name:           _Z6k_mainPKfPKDv8_DF16_S0_S3_S0_S0_S0_S0_S0_S0_S0_S0_S0_S3_S0_S0_S0_S0_S0_S0_S0_S0_S0_S0_S0_S0_S0_Pf
    .private_segment_fixed_size: 0
    .sgpr_count:     78
    .sgpr_spill_count: 0
    .symbol:         _Z6k_mainPKfPKDv8_DF16_S0_S3_S0_S0_S0_S0_S0_S0_S0_S0_S0_S3_S0_S0_S0_S0_S0_S0_S0_S0_S0_S0_S0_S0_S0_Pf.kd
    .uniform_work_group_size: 1
    .uses_dynamic_stack: false
    .vgpr_count:     128
    .vgpr_spill_count: 0
    .wavefront_size: 64
